# P5 ml_out decay weights: 32 exec-masked branch blocks replaced by batched LDS reads, SALU mask select and unconditional compute with v_cndmask (strategy 9: branch shortening on a serial chain)
# speedup vs baseline: 1.0037x; 1.0037x over previous
.LBB0_844:
	s_lshl_b32 s50, s54, 10
	s_add_i32 s50, s33, s50
	s_ashr_i32 s51, s50, 31
	s_lshl_b64 s[52:53], s[50:51], 14
	v_lshl_add_u64 v[58:59], v[158:159], 0, s[52:53]
	v_lshl_add_u64 v[60:61], v[58:59], 0, v[154:155]
	v_mov_b32_e32 v163, v155
	global_load_dwordx4 v[126:129], v[60:61], off
	global_load_dwordx4 v[122:125], v[60:61], off offset:64
	global_load_dwordx4 v[114:117], v[60:61], off offset:2048
	global_load_dwordx4 v[110:113], v[60:61], off offset:2112
	v_lshl_add_u64 v[60:61], v[58:59], 0, v[162:163]
	v_mov_b32_e32 v165, v155
	global_load_dwordx4 v[106:109], v[60:61], off
	global_load_dwordx4 v[102:105], v[60:61], off offset:64
	v_lshl_add_u64 v[60:61], v[58:59], 0, v[164:165]
	v_mov_b32_e32 v167, v155
	global_load_dwordx4 v[98:101], v[60:61], off
	global_load_dwordx4 v[94:97], v[60:61], off offset:64
	v_lshl_add_u64 v[60:61], v[58:59], 0, v[166:167]
	v_mov_b32_e32 v169, v155
	global_load_dwordx4 v[86:89], v[60:61], off
	global_load_dwordx4 v[82:85], v[60:61], off offset:64
	v_lshl_add_u64 v[60:61], v[58:59], 0, v[168:169]
	v_mov_b32_e32 v171, v155
	v_mov_b32_e32 v173, v155
	global_load_dwordx4 v[78:81], v[60:61], off
	global_load_dwordx4 v[74:77], v[60:61], off offset:64
	v_lshl_add_u64 v[60:61], v[58:59], 0, v[170:171]
	v_lshl_add_u64 v[58:59], v[58:59], 0, v[172:173]
	global_load_dwordx4 v[70:73], v[60:61], off
	global_load_dwordx4 v[66:69], v[60:61], off offset:64
	global_load_dwordx4 v[62:65], v[58:59], off
	s_nop 0
	global_load_dwordx4 v[58:61], v[58:59], off offset:64
	s_mul_i32 s52, s54, 0x600
	s_add_i32 s52, s52, 0
	s_mul_i32 s53, s54, 0xfffffa04
	s_add_i32 s53, s52, s53
	v_mov_b32_e32 v90, s53
	v_lshl_add_u32 v142, v208, 2, s52
	ds_read_b32 v143, v90 offset:37888
	ds_read_b32 v90, v142 offset:35840
	v_lshl_add_u32 v135, v214, 2, s52
	ds_read_b32 v134, v135 offset:35328
	ds_read_b32 v136, v135 offset:35332
	ds_read_b32 v138, v135 offset:35336
	ds_read_b32 v137, v135 offset:35340
	ds_read_b32 v140, v135 offset:35392
	ds_read_b32 v139, v135 offset:35396
	ds_read_b32 v145, v135 offset:35400
	ds_read_b32 v141, v135 offset:35404
	ds_read_b32 v147, v135 offset:35456
	ds_read_b32 v146, v135 offset:35460
	ds_read_b32 v149, v135 offset:35464
	ds_read_b32 v148, v135 offset:35468
	ds_read_b32 v165, v135 offset:35520
	ds_read_b32 v163, v135 offset:35524
	ds_read_b32 v169, v135 offset:35528
	ds_read_b32 v167, v135 offset:35532
	ds_read_b32 v173, v135 offset:35584
	ds_read_b32 v171, v135 offset:35588
	ds_read_b32 v239, v135 offset:35592
	ds_read_b32 v238, v135 offset:35596
	ds_read_b32 v243, v135 offset:35648
	ds_read_b32 v242, v135 offset:35652
	ds_read_b32 v248, v135 offset:35656
	ds_read_b32 v246, v135 offset:35660
	ds_read_b32 v241, v135 offset:35712
	ds_read_b32 v240, v135 offset:35716
	ds_read_b32 v245, v135 offset:35720
	ds_read_b32 v244, v135 offset:35724
	ds_read_b32 v249, v135 offset:35776
	ds_read_b32 v247, v135 offset:35780
	ds_read_b32 v251, v135 offset:35784
	ds_read_b32 v250, v135 offset:35788
	s_waitcnt lgkmcnt(1)
	v_max_f32_e32 v91, v143, v143
	s_waitcnt lgkmcnt(0)
	v_max_f32_e32 v90, v90, v90
	v_max_f32_e32 v144, v91, v90
	s_nop 0
	v_readlane_b32 s52, v253, 29
	v_readlane_b32 s53, v253, 30
	v_readlane_b32 s56, v253, 25
	v_readlane_b32 s57, v253, 26
	s_cmp_lg_u64 s[76:77], 0
	s_cselect_b64 vcc, s[52:53], s[56:57]
	s_waitcnt lgkmcnt(0)
	v_sub_f32_e32 v134, v134, v144
	v_min_f32_e32 v134, 0, v134
	v_mul_f32_e32 v134, 0x3fb8aa3b, v134
	v_exp_f32_e32 v134, v134
	s_nop 0
	v_mul_f32_e32 v134, v26, v134
	v_cndmask_b32_e32 v134, 0, v134, vcc
	s_nop 0
	s_nop 1
	v_readlane_b32 s52, v253, 51
	v_readlane_b32 s53, v253, 52
	v_readlane_b32 s56, v253, 14
	v_readlane_b32 s57, v253, 15
	s_cmp_lg_u64 s[76:77], 0
	s_cselect_b64 vcc, s[52:53], s[56:57]
	v_sub_f32_e32 v136, v136, v144
	v_min_f32_e32 v136, 0, v136
	v_mul_f32_e32 v136, 0x3fb8aa3b, v136
	v_exp_f32_e32 v136, v136
	s_nop 0
	v_mul_f32_e32 v136, v27, v136
	v_cndmask_b32_e32 v136, 0, v136, vcc
	s_nop 1
	v_readlane_b32 s52, v253, 55
	v_readlane_b32 s53, v253, 56
	v_readlane_b32 s56, v253, 53
	v_readlane_b32 s57, v253, 54
	s_cmp_lg_u64 s[76:77], 0
	s_cselect_b64 vcc, s[52:53], s[56:57]
	v_sub_f32_e32 v138, v138, v144
	v_min_f32_e32 v138, 0, v138
	v_mul_f32_e32 v138, 0x3fb8aa3b, v138
	v_exp_f32_e32 v138, v138
	s_nop 0
	v_mul_f32_e32 v138, v28, v138
	v_cndmask_b32_e32 v138, 0, v138, vcc
	s_nop 1
	s_nop 1
	v_readlane_b32 s52, v253, 59
	v_readlane_b32 s53, v253, 60
	v_readlane_b32 s56, v253, 57
	v_readlane_b32 s57, v253, 58
	s_cmp_lg_u64 s[76:77], 0
	s_cselect_b64 vcc, s[52:53], s[56:57]
	v_sub_f32_e32 v137, v137, v144
	v_min_f32_e32 v137, 0, v137
	v_mul_f32_e32 v137, 0x3fb8aa3b, v137
	v_exp_f32_e32 v137, v137
	s_nop 0
	v_mul_f32_e32 v137, v29, v137
	v_cndmask_b32_e32 v137, 0, v137, vcc
	s_nop 1
	v_readlane_b32 s52, v253, 63
	v_readlane_b32 s53, v254, 0
	v_readlane_b32 s56, v253, 61
	v_readlane_b32 s57, v253, 62
	s_cmp_lg_u64 s[76:77], 0
	s_cselect_b64 vcc, s[52:53], s[56:57]
	v_sub_f32_e32 v140, v140, v144
	v_min_f32_e32 v140, 0, v140
	v_mul_f32_e32 v140, 0x3fb8aa3b, v140
	v_exp_f32_e32 v140, v140
	s_nop 0
	v_mul_f32_e32 v140, v30, v140
	v_cndmask_b32_e32 v140, 0, v140, vcc
	s_nop 1
	s_nop 1
	v_readlane_b32 s52, v254, 3
	v_readlane_b32 s53, v254, 4
	v_readlane_b32 s56, v254, 1
	v_readlane_b32 s57, v254, 2
	s_cmp_lg_u64 s[76:77], 0
	s_cselect_b64 vcc, s[52:53], s[56:57]
	v_sub_f32_e32 v139, v139, v144
	v_min_f32_e32 v139, 0, v139
	v_mul_f32_e32 v139, 0x3fb8aa3b, v139
	v_exp_f32_e32 v139, v139
	s_nop 0
	v_mul_f32_e32 v139, v31, v139
	v_cndmask_b32_e32 v139, 0, v139, vcc
	s_nop 1
	v_readlane_b32 s52, v254, 7
	v_readlane_b32 s53, v254, 8
	v_readlane_b32 s56, v254, 5
	v_readlane_b32 s57, v254, 6
	s_cmp_lg_u64 s[76:77], 0
	s_cselect_b64 vcc, s[52:53], s[56:57]
	v_sub_f32_e32 v145, v145, v144
	v_min_f32_e32 v145, 0, v145
	v_mul_f32_e32 v145, 0x3fb8aa3b, v145
	v_exp_f32_e32 v145, v145
	s_nop 0
	v_mul_f32_e32 v145, v32, v145
	v_cndmask_b32_e32 v145, 0, v145, vcc
	s_nop 1
	s_nop 1
	v_readlane_b32 s52, v254, 11
	v_readlane_b32 s53, v254, 12
	v_readlane_b32 s56, v254, 9
	v_readlane_b32 s57, v254, 10
	s_cmp_lg_u64 s[76:77], 0
	s_cselect_b64 vcc, s[52:53], s[56:57]
	v_sub_f32_e32 v141, v141, v144
	v_min_f32_e32 v141, 0, v141
	v_mul_f32_e32 v141, 0x3fb8aa3b, v141
	v_exp_f32_e32 v141, v141
	s_nop 0
	v_mul_f32_e32 v141, v33, v141
	v_cndmask_b32_e32 v141, 0, v141, vcc
	v_cvt_pk_bf16_f32 v90, v134, v136
	v_cvt_pk_bf16_f32 v91, v138, v137
	v_cvt_pk_bf16_f32 v92, v140, v139
	v_cvt_pk_bf16_f32 v93, v145, v141
	s_nop 1
	v_readlane_b32 s52, v254, 15
	v_readlane_b32 s53, v254, 16
	v_readlane_b32 s56, v254, 13
	v_readlane_b32 s57, v254, 14
	s_cmp_lg_u64 s[76:77], 0
	s_cselect_b64 vcc, s[52:53], s[56:57]
	v_sub_f32_e32 v147, v147, v144
	v_min_f32_e32 v147, 0, v147
	v_mul_f32_e32 v147, 0x3fb8aa3b, v147
	v_exp_f32_e32 v147, v147
	s_nop 0
	v_mul_f32_e32 v147, v34, v147
	v_cndmask_b32_e32 v147, 0, v147, vcc
	s_nop 1
	s_nop 1
	v_readlane_b32 s52, v254, 19
	v_readlane_b32 s53, v254, 20
	v_readlane_b32 s56, v254, 17
	v_readlane_b32 s57, v254, 18
	s_cmp_lg_u64 s[76:77], 0
	s_cselect_b64 vcc, s[52:53], s[56:57]
	v_sub_f32_e32 v146, v146, v144
	v_min_f32_e32 v146, 0, v146
	v_mul_f32_e32 v146, 0x3fb8aa3b, v146
	v_exp_f32_e32 v146, v146
	s_nop 0
	v_mul_f32_e32 v146, v35, v146
	v_cndmask_b32_e32 v146, 0, v146, vcc
	s_nop 1
	v_readlane_b32 s52, v254, 23
	v_readlane_b32 s53, v254, 24
	v_readlane_b32 s56, v254, 21
	v_readlane_b32 s57, v254, 22
	s_cmp_lg_u64 s[76:77], 0
	s_cselect_b64 vcc, s[52:53], s[56:57]
	v_sub_f32_e32 v149, v149, v144
	v_min_f32_e32 v149, 0, v149
	v_mul_f32_e32 v149, 0x3fb8aa3b, v149
	v_exp_f32_e32 v149, v149
	s_nop 0
	v_mul_f32_e32 v149, v36, v149
	v_cndmask_b32_e32 v149, 0, v149, vcc
	s_nop 1
	s_nop 1
	v_readlane_b32 s52, v254, 27
	v_readlane_b32 s53, v254, 28
	v_readlane_b32 s56, v254, 25
	v_readlane_b32 s57, v254, 26
	s_cmp_lg_u64 s[76:77], 0
	s_cselect_b64 vcc, s[52:53], s[56:57]
	v_sub_f32_e32 v148, v148, v144
	v_min_f32_e32 v148, 0, v148
	v_mul_f32_e32 v148, 0x3fb8aa3b, v148
	v_exp_f32_e32 v148, v148
	s_nop 0
	v_mul_f32_e32 v148, v37, v148
	v_cndmask_b32_e32 v148, 0, v148, vcc
	s_nop 1
	v_readlane_b32 s52, v254, 31
	v_readlane_b32 s53, v254, 32
	v_readlane_b32 s56, v254, 29
	v_readlane_b32 s57, v254, 30
	s_cmp_lg_u64 s[76:77], 0
	s_cselect_b64 vcc, s[52:53], s[56:57]
	v_sub_f32_e32 v165, v165, v144
	v_min_f32_e32 v165, 0, v165
	v_mul_f32_e32 v165, 0x3fb8aa3b, v165
	v_exp_f32_e32 v165, v165
	s_nop 0
	v_mul_f32_e32 v165, v38, v165
	v_cndmask_b32_e32 v165, 0, v165, vcc
	s_nop 1
	s_nop 1
	v_readlane_b32 s52, v254, 35
	v_readlane_b32 s53, v254, 36
	v_readlane_b32 s56, v254, 33
	v_readlane_b32 s57, v254, 34
	s_cmp_lg_u64 s[76:77], 0
	s_cselect_b64 vcc, s[52:53], s[56:57]
	v_sub_f32_e32 v163, v163, v144
	v_min_f32_e32 v163, 0, v163
	v_mul_f32_e32 v163, 0x3fb8aa3b, v163
	v_exp_f32_e32 v163, v163
	s_nop 0
	v_mul_f32_e32 v163, v39, v163
	v_cndmask_b32_e32 v163, 0, v163, vcc
	s_nop 1
	v_readlane_b32 s52, v254, 39
	v_readlane_b32 s53, v254, 40
	v_readlane_b32 s56, v254, 37
	v_readlane_b32 s57, v254, 38
	s_cmp_lg_u64 s[76:77], 0
	s_cselect_b64 vcc, s[52:53], s[56:57]
	v_sub_f32_e32 v169, v169, v144
	v_min_f32_e32 v169, 0, v169
	v_mul_f32_e32 v169, 0x3fb8aa3b, v169
	v_exp_f32_e32 v169, v169
	s_nop 0
	v_mul_f32_e32 v169, v40, v169
	v_cndmask_b32_e32 v169, 0, v169, vcc
	s_nop 1
	s_nop 1
	v_readlane_b32 s52, v254, 43
	v_readlane_b32 s53, v254, 44
	v_readlane_b32 s56, v254, 41
	v_readlane_b32 s57, v254, 42
	s_cmp_lg_u64 s[76:77], 0
	s_cselect_b64 vcc, s[52:53], s[56:57]
	v_sub_f32_e32 v167, v167, v144
	v_min_f32_e32 v167, 0, v167
	v_mul_f32_e32 v167, 0x3fb8aa3b, v167
	v_exp_f32_e32 v167, v167
	s_nop 0
	v_mul_f32_e32 v167, v41, v167
	v_cndmask_b32_e32 v167, 0, v167, vcc
	v_cvt_pk_bf16_f32 v118, v147, v146
	v_cvt_pk_bf16_f32 v119, v149, v148
	v_cvt_pk_bf16_f32 v120, v165, v163
	v_cvt_pk_bf16_f32 v121, v169, v167
	s_nop 1
	v_readlane_b32 s52, v254, 47
	v_readlane_b32 s53, v254, 48
	v_readlane_b32 s56, v254, 45
	v_readlane_b32 s57, v254, 46
	s_cmp_lg_u64 s[76:77], 0
	s_cselect_b64 vcc, s[52:53], s[56:57]
	v_sub_f32_e32 v173, v173, v144
	v_min_f32_e32 v173, 0, v173
	v_mul_f32_e32 v173, 0x3fb8aa3b, v173
	v_exp_f32_e32 v173, v173
	s_nop 0
	v_mul_f32_e32 v173, v42, v173
	v_cndmask_b32_e32 v173, 0, v173, vcc
	s_nop 1
	s_nop 1
	v_readlane_b32 s52, v254, 51
	v_readlane_b32 s53, v254, 52
	v_readlane_b32 s56, v254, 49
	v_readlane_b32 s57, v254, 50
	s_cmp_lg_u64 s[76:77], 0
	s_cselect_b64 vcc, s[52:53], s[56:57]
	v_sub_f32_e32 v171, v171, v144
	v_min_f32_e32 v171, 0, v171
	v_mul_f32_e32 v171, 0x3fb8aa3b, v171
	v_exp_f32_e32 v171, v171
	s_nop 0
	v_mul_f32_e32 v171, v43, v171
	v_cndmask_b32_e32 v171, 0, v171, vcc
	s_nop 1
	v_readlane_b32 s52, v254, 55
	v_readlane_b32 s53, v254, 56
	v_readlane_b32 s56, v254, 53
	v_readlane_b32 s57, v254, 54
	s_cmp_lg_u64 s[76:77], 0
	s_cselect_b64 vcc, s[52:53], s[56:57]
	v_sub_f32_e32 v239, v239, v144
	v_min_f32_e32 v239, 0, v239
	v_mul_f32_e32 v239, 0x3fb8aa3b, v239
	v_exp_f32_e32 v239, v239
	s_nop 0
	v_mul_f32_e32 v239, v44, v239
	v_cndmask_b32_e32 v239, 0, v239, vcc
	s_cmp_lg_u64 s[76:77], 0
	s_cselect_b64 vcc, s[94:95], s[92:93]
	v_sub_f32_e32 v238, v238, v144
	v_min_f32_e32 v238, 0, v238
	v_mul_f32_e32 v238, 0x3fb8aa3b, v238
	v_exp_f32_e32 v238, v238
	s_nop 0
	v_mul_f32_e32 v238, v45, v238
	v_cndmask_b32_e32 v238, 0, v238, vcc
	s_cmp_lg_u64 s[76:77], 0
	s_cselect_b64 vcc, s[4:5], s[96:97]
	v_sub_f32_e32 v243, v243, v144
	v_min_f32_e32 v243, 0, v243
	v_mul_f32_e32 v243, 0x3fb8aa3b, v243
	v_exp_f32_e32 v243, v243
	s_nop 0
	v_mul_f32_e32 v243, v46, v243
	v_cndmask_b32_e32 v243, 0, v243, vcc
	s_cmp_lg_u64 s[76:77], 0
	s_cselect_b64 vcc, s[8:9], s[6:7]
	v_sub_f32_e32 v242, v242, v144
	v_min_f32_e32 v242, 0, v242
	v_mul_f32_e32 v242, 0x3fb8aa3b, v242
	v_exp_f32_e32 v242, v242
	s_nop 0
	v_mul_f32_e32 v242, v47, v242
	v_cndmask_b32_e32 v242, 0, v242, vcc
	s_cmp_lg_u64 s[76:77], 0
	s_cselect_b64 vcc, s[0:1], s[12:13]
	v_sub_f32_e32 v248, v248, v144
	v_min_f32_e32 v248, 0, v248
	v_mul_f32_e32 v248, 0x3fb8aa3b, v248
	v_exp_f32_e32 v248, v248
	s_nop 0
	v_mul_f32_e32 v248, v48, v248
	v_cndmask_b32_e32 v248, 0, v248, vcc
	s_cmp_lg_u64 s[76:77], 0
	s_cselect_b64 vcc, s[14:15], s[2:3]
	v_sub_f32_e32 v246, v246, v144
	v_min_f32_e32 v246, 0, v246
	v_mul_f32_e32 v246, 0x3fb8aa3b, v246
	v_exp_f32_e32 v246, v246
	s_nop 0
	v_mul_f32_e32 v246, v49, v246
	v_cndmask_b32_e32 v246, 0, v246, vcc
	v_cvt_pk_bf16_f32 v130, v173, v171
	v_cvt_pk_bf16_f32 v131, v239, v238
	v_cvt_pk_bf16_f32 v132, v243, v242
	v_cvt_pk_bf16_f32 v133, v248, v246
	s_cmp_lg_u64 s[76:77], 0
	s_cselect_b64 vcc, s[18:19], s[16:17]
	v_sub_f32_e32 v241, v241, v144
	v_min_f32_e32 v241, 0, v241
	v_mul_f32_e32 v241, 0x3fb8aa3b, v241
	v_exp_f32_e32 v241, v241
	s_nop 0
	v_mul_f32_e32 v241, v50, v241
	v_cndmask_b32_e32 v241, 0, v241, vcc
	s_cmp_lg_u64 s[76:77], 0
	s_cselect_b64 vcc, s[22:23], s[20:21]
	v_sub_f32_e32 v240, v240, v144
	v_min_f32_e32 v240, 0, v240
	v_mul_f32_e32 v240, 0x3fb8aa3b, v240
	v_exp_f32_e32 v240, v240
	s_nop 0
	v_mul_f32_e32 v240, v51, v240
	v_cndmask_b32_e32 v240, 0, v240, vcc
	s_cmp_lg_u64 s[76:77], 0
	s_cselect_b64 vcc, s[26:27], s[24:25]
	v_sub_f32_e32 v245, v245, v144
	v_min_f32_e32 v245, 0, v245
	v_mul_f32_e32 v245, 0x3fb8aa3b, v245
	v_exp_f32_e32 v245, v245
	s_nop 0
	v_mul_f32_e32 v245, v52, v245
	v_cndmask_b32_e32 v245, 0, v245, vcc
	s_cmp_lg_u64 s[76:77], 0
	s_cselect_b64 vcc, s[30:31], s[28:29]
	v_sub_f32_e32 v244, v244, v144
	v_min_f32_e32 v244, 0, v244
	v_mul_f32_e32 v244, 0x3fb8aa3b, v244
	v_exp_f32_e32 v244, v244
	s_nop 0
	v_mul_f32_e32 v244, v53, v244
	v_cndmask_b32_e32 v244, 0, v244, vcc
	s_cmp_lg_u64 s[76:77], 0
	s_cselect_b64 vcc, s[36:37], s[34:35]
	v_sub_f32_e32 v249, v249, v144
	v_min_f32_e32 v249, 0, v249
	v_mul_f32_e32 v249, 0x3fb8aa3b, v249
	v_exp_f32_e32 v249, v249
	s_nop 0
	v_mul_f32_e32 v249, v54, v249
	v_cndmask_b32_e32 v249, 0, v249, vcc
	s_cmp_lg_u64 s[76:77], 0
	s_cselect_b64 vcc, s[40:41], s[38:39]
	v_sub_f32_e32 v247, v247, v144
	v_min_f32_e32 v247, 0, v247
	v_mul_f32_e32 v247, 0x3fb8aa3b, v247
	v_exp_f32_e32 v247, v247
	s_nop 0
	v_mul_f32_e32 v247, v55, v247
	v_cndmask_b32_e32 v247, 0, v247, vcc
	s_cmp_lg_u64 s[76:77], 0
	s_cselect_b64 vcc, s[44:45], s[42:43]
	v_sub_f32_e32 v251, v251, v144
	v_min_f32_e32 v251, 0, v251
	v_mul_f32_e32 v251, 0x3fb8aa3b, v251
	v_exp_f32_e32 v251, v251
	s_nop 0
	v_mul_f32_e32 v251, v56, v251
	v_cndmask_b32_e32 v251, 0, v251, vcc
	s_cmp_lg_u64 s[76:77], 0
	s_cselect_b64 vcc, s[48:49], s[46:47]
	v_sub_f32_e32 v250, v250, v144
	v_min_f32_e32 v250, 0, v250
	v_mul_f32_e32 v250, 0x3fb8aa3b, v250
	v_exp_f32_e32 v250, v250
	s_nop 0
	v_mul_f32_e32 v250, v57, v250
	v_cndmask_b32_e32 v250, 0, v250, vcc
	v_add_f32_e32 v1, 0, v134
	v_add_f32_e32 v1, v1, v136
	v_add_f32_e32 v1, v1, v138
	v_add_f32_e32 v1, v1, v137
	v_add_f32_e32 v1, v1, v140
	v_add_f32_e32 v1, v1, v139
	v_add_f32_e32 v1, v1, v145
	v_add_f32_e32 v1, v1, v141
	v_add_f32_e32 v1, v1, v147
	v_add_f32_e32 v1, v1, v146
	v_add_f32_e32 v1, v1, v149
	v_add_f32_e32 v1, v1, v148
	v_add_f32_e32 v1, v1, v165
	v_add_f32_e32 v1, v1, v163
	v_add_f32_e32 v1, v1, v169
	v_add_f32_e32 v1, v1, v167
	v_add_f32_e32 v1, v1, v173
	v_add_f32_e32 v1, v1, v171
	v_add_f32_e32 v1, v1, v239
	v_add_f32_e32 v1, v1, v238
	v_add_f32_e32 v1, v1, v243
	v_add_f32_e32 v1, v1, v242
	v_add_f32_e32 v1, v1, v248
	v_add_f32_e32 v1, v1, v246
	v_add_f32_e32 v1, v1, v241
	v_add_f32_e32 v1, v1, v240
	v_add_f32_e32 v1, v1, v245
	v_add_f32_e32 v1, v1, v244
	v_and_b32_e32 v139, 64, v219
	v_add_f32_e32 v1, v1, v249
	v_xor_b32_e32 v138, 16, v219
	v_add_u32_e32 v163, 64, v139
	v_add_f32_e32 v1, v1, v247
	v_cmp_lt_i32_e32 vcc, v138, v163
	v_add_f32_e32 v1, v1, v251
	v_add_f32_e32 v1, v1, v250
	v_cndmask_b32_e32 v138, v219, v138, vcc
	v_lshlrev_b32_e32 v147, 2, v138
	ds_bpermute_b32 v138, v147, v1
	s_lshl_b64 s[50:51], s[50:51], 8
	v_lshl_add_u64 v[148:149], v[160:161], 0, s[50:51]
	v_cvt_pk_bf16_f32 v134, v241, v240
	v_cvt_pk_bf16_f32 v135, v245, v244
	v_cvt_pk_bf16_f32 v136, v249, v247
	v_cvt_pk_bf16_f32 v137, v251, v250
	s_waitcnt lgkmcnt(0)
	v_add_f32_e32 v145, v1, v138
	global_load_dwordx4 v[138:141], v[148:149], off offset:16
	global_load_dwordx4 v[238:241], v[148:149], off
	v_xor_b32_e32 v1, 32, v219
	v_cmp_lt_i32_e32 vcc, v1, v163
	s_lshl_b32 s50, s54, 7
	v_readlane_b32 s51, v253, 24
	v_cndmask_b32_e32 v1, v219, v1, vcc
	v_lshlrev_b32_e32 v1, 2, v1
	ds_bpermute_b32 v146, v1, v145
	s_add_i32 s52, s51, s50
	s_waitcnt vmcnt(1)
	v_mul_f32_e32 v139, v139, v227
	s_waitcnt vmcnt(0)
	v_mul_f32_e32 v165, v239, v223
	v_fmac_f32_e32 v165, v238, v151
	v_mul_f32_e32 v167, v241, v225
	v_add_f32_e32 v165, 0, v165
	v_fmac_f32_e32 v167, v240, v224
	v_add_f32_e32 v165, v165, v167
	v_fmac_f32_e32 v139, v138, v226
	v_add_f32_e32 v138, v165, v139
	v_mul_f32_e32 v139, v141, v229
	v_fmac_f32_e32 v139, v140, v228
	v_add_f32_e32 v165, v138, v139
	global_load_dwordx4 v[138:141], v[148:149], off offset:144
	global_load_dwordx4 v[238:241], v[148:149], off offset:128
	s_waitcnt vmcnt(1)
	v_mul_f32_e32 v139, v139, v235
	s_waitcnt vmcnt(0)
	v_mul_f32_e32 v148, v239, v231
	v_fmac_f32_e32 v148, v238, v230
	v_mul_f32_e32 v149, v241, v233
	v_add_f32_e32 v148, v165, v148
	v_fmac_f32_e32 v149, v240, v232
	v_add_f32_e32 v148, v148, v149
	v_fmac_f32_e32 v139, v138, v234
	v_add_f32_e32 v138, v148, v139
	v_mul_f32_e32 v139, v141, v237
	v_fmac_f32_e32 v139, v140, v236
	v_add_f32_e32 v138, v138, v139
	ds_bpermute_b32 v139, v147, v138
	s_waitcnt lgkmcnt(0)
	v_add_f32_e32 v138, v138, v139
	ds_bpermute_b32 v139, v1, v138
	s_and_saveexec_b64 s[50:51], s[10:11]
	s_cbranch_execz .LBB0_910
	ds_read_b32 v1, v142 offset:34816
	v_sub_f32_e32 v140, v143, v144
	v_mul_f32_e32 v140, 0x3fb8aa3b, v140
	v_exp_f32_e32 v140, v140
	v_add_f32_e32 v141, v145, v146
	s_waitcnt lgkmcnt(0)
	v_add_f32_e32 v1, v144, v1
	v_mul_f32_e32 v1, 0xbfb8aa3b, v1
	v_exp_f32_e32 v1, v1
	v_add_f32_e32 v138, v138, v139
	v_fmac_f32_e32 v141, v140, v138
	v_max_f32_e64 v1, |v141|, v1
	v_div_scale_f32 v138, s[54:55], v1, v1, 1.0
	v_rcp_f32_e32 v139, v138
	v_div_scale_f32 v141, vcc, 1.0, v1, 1.0
	v_fma_f32 v142, -v138, v139, 1.0
	v_fmac_f32_e32 v139, v142, v139
	v_mul_f32_e32 v142, v141, v139
	v_fma_f32 v143, -v138, v142, v141
	v_fmac_f32_e32 v142, v143, v139
	v_fma_f32 v138, -v138, v142, v141
	v_div_fmas_f32 v138, v138, v139, v142
	v_div_fixup_f32 v1, v138, v1, 1.0
	v_lshl_add_u32 v138, v153, 2, s52
	ds_write_b32 v138, v1 offset:37904
	v_lshl_add_u32 v1, v206, 2, s52
	ds_write_b32 v1, v140 offset:37968
